# two barriers per attention unit (next unit's V blocks waited for at the post-K-loop barrier) with the unit-1 priority raise
# baseline (speedup 1.0000x reference)
.LBB0_431:
	s_cmp_lt_i32 s33, 1
	s_cselect_b64 s[78:79], -1, 0
	s_lshl_b32 s37, s88, 6
	ds_read_b128 v[82:85], v221 offset:32768
	ds_read_b128 v[86:89], v222 offset:32768
	ds_read_b128 v[90:93], v223 offset:32768
	ds_read_b128 v[94:97], v224 offset:32768
	ds_read_b128 v[98:101], v221 offset:36864
	ds_read_b128 v[102:105], v222 offset:36864
	ds_read_b128 v[106:109], v223 offset:36864
	ds_read_b128 v[110:113], v224 offset:36864
	s_waitcnt lgkmcnt(7)
	v_mfma_f32_32x32x16_bf16 v[18:33], v[82:85], v[158:161], 0
	s_waitcnt lgkmcnt(6)
	v_mfma_f32_32x32x16_bf16 v[18:33], v[86:89], v[154:157], v[18:33]
	s_waitcnt lgkmcnt(5)
	v_mfma_f32_32x32x16_bf16 v[18:33], v[90:93], v[150:153], v[18:33]
	s_waitcnt lgkmcnt(4)
	v_mfma_f32_32x32x16_bf16 v[18:33], v[94:97], v[146:149], v[18:33]
	ds_read_b128 v[82:85], v221 offset:40960
	ds_read_b128 v[86:89], v222 offset:40960
	ds_read_b128 v[90:93], v223 offset:40960
	ds_read_b128 v[94:97], v224 offset:40960
	s_waitcnt lgkmcnt(7)
	v_mfma_f32_32x32x16_bf16 v[2:17], v[98:101], v[158:161], 0
	s_waitcnt lgkmcnt(6)
	v_mfma_f32_32x32x16_bf16 v[2:17], v[102:105], v[154:157], v[2:17]
	s_waitcnt lgkmcnt(5)
	v_mfma_f32_32x32x16_bf16 v[2:17], v[106:109], v[150:153], v[2:17]
	s_waitcnt lgkmcnt(4)
	v_mfma_f32_32x32x16_bf16 v[2:17], v[110:113], v[146:149], v[2:17]
	ds_read_b128 v[98:101], v221 offset:45056
	ds_read_b128 v[102:105], v222 offset:45056
	ds_read_b128 v[106:109], v223 offset:45056
	ds_read_b128 v[110:113], v224 offset:45056
	s_waitcnt lgkmcnt(7)
	v_mfma_f32_32x32x16_bf16 v[34:49], v[82:85], v[158:161], 0
	s_waitcnt lgkmcnt(6)
	v_mfma_f32_32x32x16_bf16 v[34:49], v[86:89], v[154:157], v[34:49]
	s_waitcnt lgkmcnt(5)
	v_mfma_f32_32x32x16_bf16 v[34:49], v[90:93], v[150:153], v[34:49]
	s_waitcnt lgkmcnt(4)
	v_mfma_f32_32x32x16_bf16 v[34:49], v[94:97], v[146:149], v[34:49]
	ds_read_b128 v[82:85], v221 offset:49152
	ds_read_b128 v[86:89], v222 offset:49152
	ds_read_b128 v[90:93], v223 offset:49152
	ds_read_b128 v[94:97], v224 offset:49152
	s_waitcnt lgkmcnt(7)
	v_mfma_f32_32x32x16_bf16 v[50:65], v[98:101], v[158:161], 0
	s_waitcnt lgkmcnt(6)
	v_mfma_f32_32x32x16_bf16 v[50:65], v[102:105], v[154:157], v[50:65]
	s_waitcnt lgkmcnt(5)
	v_mfma_f32_32x32x16_bf16 v[50:65], v[106:109], v[150:153], v[50:65]
	s_waitcnt lgkmcnt(4)
	v_mfma_f32_32x32x16_bf16 v[50:65], v[110:113], v[146:149], v[50:65]
	s_waitcnt lgkmcnt(3)
	v_mfma_f32_32x32x16_bf16 v[66:81], v[82:85], v[158:161], 0
	s_waitcnt lgkmcnt(2)
	v_mfma_f32_32x32x16_bf16 v[66:81], v[86:89], v[154:157], v[66:81]
	s_waitcnt lgkmcnt(1)
	v_mfma_f32_32x32x16_bf16 v[66:81], v[90:93], v[150:153], v[66:81]
	s_waitcnt lgkmcnt(0)
	v_mfma_f32_32x32x16_bf16 v[66:81], v[94:97], v[146:149], v[66:81]
	s_waitcnt vmcnt(0)
	s_barrier
	s_add_i32 s38, s53, 1
	s_cmp_lt_i32 s38, s0
	s_cselect_b64 s[96:97], -1, 0
	s_cmp_ge_i32 s38, s0
	s_mov_b32 s39, s86
	s_mov_b32 s40, s88
	s_mov_b32 s47, s81
	s_mov_b32 s41, s33
	s_mov_b32 s80, s42
	s_mov_b32 s48, s82
	v_mov_b32_e32 v183, v180
	v_mov_b32_e32 v190, v178
	v_mov_b32_e32 v187, v182
	s_cbranch_scc1 .LBB0_466
	v_readlane_b32 s40, v254, 8
	v_readlane_b32 s41, v254, 9
	s_mov_b64 s[4:5], -1
	s_and_b64 vcc, exec, s[40:41]
	s_cbranch_vccz .LBB0_454
	s_mul_i32 s4, s38, s74
	v_readlane_b32 s40, v254, 19
	s_add_i32 s39, s4, s40
	s_mov_b64 s[4:5], 0

.LBB0_471:
	v_cndmask_b32_e64 v70, v81, v226, s[78:79]
	v_max3_f32 v33, v18, v97, v20
	v_max3_f32 v33, v33, v19, v22
	v_max3_f32 v33, v33, v21, v24
	v_max3_f32 v33, v33, v23, v26
	v_max3_f32 v33, v33, v25, v28
	v_max3_f32 v33, v33, v27, v31
	v_max3_f32 v33, v33, v29, v30
	v_max3_f32 v33, v33, v32, v3
	v_max3_f32 v33, v33, v2, v5
	v_max3_f32 v33, v33, v4, v7
	v_max3_f32 v33, v33, v6, v9
	v_max3_f32 v33, v33, v8, v11
	v_max3_f32 v33, v33, v10, v13
	v_max3_f32 v33, v33, v12, v15
	v_max3_f32 v33, v33, v14, v17
	v_max3_f32 v33, v33, v16, v35
	v_max3_f32 v33, v33, v34, v37
	v_max3_f32 v33, v33, v36, v39
	v_max3_f32 v33, v33, v38, v41
	v_max3_f32 v33, v33, v40, v43
	v_max3_f32 v33, v33, v42, v45
	v_max3_f32 v33, v33, v44, v47
	v_max3_f32 v33, v33, v46, v49
	v_max3_f32 v33, v33, v48, v51
	v_max3_f32 v33, v33, v50, v53
	v_max3_f32 v33, v33, v52, v55
	v_max3_f32 v33, v33, v54, v57
	v_max3_f32 v33, v33, v56, v59
	v_max3_f32 v33, v33, v58, v61
	v_max3_f32 v33, v33, v60, v63
	v_max3_f32 v33, v33, v62, v65
	v_max3_f32 v33, v33, v64, v83
	v_max3_f32 v33, v33, v82, v85
	v_max3_f32 v33, v33, v84, v87
	v_max3_f32 v33, v33, v86, v89
	v_max3_f32 v33, v33, v88, v91
	v_max3_f32 v33, v33, v90, v93
	v_max3_f32 v33, v33, v92, v95
	v_max3_f32 v33, v33, v94, v70
	v_max_f32_e32 v33, v33, v96
	v_and_b32_e32 v67, 64, v209
	v_xor_b32_e32 v66, 32, v209
	v_add_u32_e32 v67, 64, v67
	v_cmp_lt_i32_e32 vcc, v66, v67
	s_nop 1
	v_cndmask_b32_e32 v66, v209, v66, vcc
	v_lshlrev_b32_e32 v118, 2, v66
	ds_bpermute_b32 v66, v118, v33
	s_waitcnt lgkmcnt(0)
	v_max_f32_e32 v66, v33, v66
	v_pk_add_f32 v[2:3], v[2:3], v[66:67] op_sel_hi:[1,0] neg_lo:[0,1] neg_hi:[0,1]
	v_pk_add_f32 v[4:5], v[4:5], v[66:67] op_sel_hi:[1,0] neg_lo:[0,1] neg_hi:[0,1]
	v_pk_add_f32 v[6:7], v[6:7], v[66:67] op_sel_hi:[1,0] neg_lo:[0,1] neg_hi:[0,1]
	v_pk_add_f32 v[8:9], v[8:9], v[66:67] op_sel_hi:[1,0] neg_lo:[0,1] neg_hi:[0,1]
	v_pk_add_f32 v[10:11], v[10:11], v[66:67] op_sel_hi:[1,0] neg_lo:[0,1] neg_hi:[0,1]
	v_pk_add_f32 v[12:13], v[12:13], v[66:67] op_sel_hi:[1,0] neg_lo:[0,1] neg_hi:[0,1]
	v_pk_add_f32 v[14:15], v[14:15], v[66:67] op_sel_hi:[1,0] neg_lo:[0,1] neg_hi:[0,1]
	v_pk_add_f32 v[16:17], v[16:17], v[66:67] op_sel_hi:[1,0] neg_lo:[0,1] neg_hi:[0,1]
	v_pk_add_f32 v[18:19], v[18:19], v[66:67] op_sel_hi:[1,0] neg_lo:[0,1] neg_hi:[0,1]
	v_pk_add_f32 v[20:21], v[20:21], v[66:67] op_sel_hi:[1,0] neg_lo:[0,1] neg_hi:[0,1]
	v_pk_add_f32 v[22:23], v[22:23], v[66:67] op_sel_hi:[1,0] neg_lo:[0,1] neg_hi:[0,1]
	v_pk_add_f32 v[24:25], v[24:25], v[66:67] op_sel_hi:[1,0] neg_lo:[0,1] neg_hi:[0,1]
	v_pk_add_f32 v[26:27], v[26:27], v[66:67] op_sel_hi:[1,0] neg_lo:[0,1] neg_hi:[0,1]
	v_pk_add_f32 v[28:29], v[28:29], v[66:67] op_sel_hi:[1,0] neg_lo:[0,1] neg_hi:[0,1]
	v_pk_add_f32 v[30:31], v[30:31], v[66:67] op_sel_hi:[1,0] neg_lo:[0,1] neg_hi:[0,1]
	v_pk_add_f32 v[34:35], v[34:35], v[66:67] op_sel_hi:[1,0] neg_lo:[0,1] neg_hi:[0,1]
	v_pk_add_f32 v[36:37], v[36:37], v[66:67] op_sel_hi:[1,0] neg_lo:[0,1] neg_hi:[0,1]
	v_pk_add_f32 v[38:39], v[38:39], v[66:67] op_sel_hi:[1,0] neg_lo:[0,1] neg_hi:[0,1]
	v_pk_add_f32 v[40:41], v[40:41], v[66:67] op_sel_hi:[1,0] neg_lo:[0,1] neg_hi:[0,1]
	v_pk_add_f32 v[42:43], v[42:43], v[66:67] op_sel_hi:[1,0] neg_lo:[0,1] neg_hi:[0,1]
	v_pk_add_f32 v[44:45], v[44:45], v[66:67] op_sel_hi:[1,0] neg_lo:[0,1] neg_hi:[0,1]
	v_pk_add_f32 v[46:47], v[46:47], v[66:67] op_sel_hi:[1,0] neg_lo:[0,1] neg_hi:[0,1]
	v_pk_add_f32 v[48:49], v[48:49], v[66:67] op_sel_hi:[1,0] neg_lo:[0,1] neg_hi:[0,1]
	v_pk_add_f32 v[50:51], v[50:51], v[66:67] op_sel_hi:[1,0] neg_lo:[0,1] neg_hi:[0,1]
	v_pk_add_f32 v[52:53], v[52:53], v[66:67] op_sel_hi:[1,0] neg_lo:[0,1] neg_hi:[0,1]
	v_pk_add_f32 v[54:55], v[54:55], v[66:67] op_sel_hi:[1,0] neg_lo:[0,1] neg_hi:[0,1]
	v_pk_add_f32 v[56:57], v[56:57], v[66:67] op_sel_hi:[1,0] neg_lo:[0,1] neg_hi:[0,1]
	v_pk_add_f32 v[58:59], v[58:59], v[66:67] op_sel_hi:[1,0] neg_lo:[0,1] neg_hi:[0,1]
	v_pk_add_f32 v[60:61], v[60:61], v[66:67] op_sel_hi:[1,0] neg_lo:[0,1] neg_hi:[0,1]
	v_pk_add_f32 v[62:63], v[62:63], v[66:67] op_sel_hi:[1,0] neg_lo:[0,1] neg_hi:[0,1]
	v_pk_add_f32 v[64:65], v[64:65], v[66:67] op_sel_hi:[1,0] neg_lo:[0,1] neg_hi:[0,1]
	v_pk_add_f32 v[82:83], v[82:83], v[66:67] op_sel_hi:[1,0] neg_lo:[0,1] neg_hi:[0,1]
	v_pk_add_f32 v[84:85], v[84:85], v[66:67] op_sel_hi:[1,0] neg_lo:[0,1] neg_hi:[0,1]
	v_pk_add_f32 v[86:87], v[86:87], v[66:67] op_sel_hi:[1,0] neg_lo:[0,1] neg_hi:[0,1]
	v_pk_add_f32 v[88:89], v[88:89], v[66:67] op_sel_hi:[1,0] neg_lo:[0,1] neg_hi:[0,1]
	v_pk_add_f32 v[90:91], v[90:91], v[66:67] op_sel_hi:[1,0] neg_lo:[0,1] neg_hi:[0,1]
	v_pk_add_f32 v[92:93], v[92:93], v[66:67] op_sel_hi:[1,0] neg_lo:[0,1] neg_hi:[0,1]
	v_pk_add_f32 v[94:95], v[94:95], v[66:67] op_sel_hi:[1,0] neg_lo:[0,1] neg_hi:[0,1]
	v_pk_add_f32 v[96:97], v[96:97], v[66:67] op_sel_hi:[1,0] neg_lo:[0,1] neg_hi:[0,1]
	v_sub_f32_e32 v32, v32, v66
	v_sub_f32_e32 v70, v70, v66
	v_exp_f32_e32 v33, v97
	v_exp_f32_e32 v18, v18
	v_exp_f32_e32 v19, v19
	v_exp_f32_e32 v20, v20
	v_mov_b32_e32 v244, 0
	v_mov_b32_e32 v245, 0
	v_add_f32_e32 v244, v33, v244
	v_exp_f32_e32 v21, v21
	v_exp_f32_e32 v22, v22
	v_pk_add_f32 v[244:245], v[18:19], v[244:245]
	v_exp_f32_e32 v23, v23
	v_exp_f32_e32 v24, v24
	v_pk_add_f32 v[244:245], v[20:21], v[244:245]
	v_exp_f32_e32 v119, v25
	v_exp_f32_e32 v120, v26
	v_pk_add_f32 v[244:245], v[22:23], v[244:245]
	v_exp_f32_e32 v121, v27
	v_add_f32_e32 v244, v24, v244
	v_exp_f32_e32 v122, v28
	v_add_f32_e32 v244, v119, v244
	v_exp_f32_e32 v123, v29
	v_exp_f32_e32 v124, v31
	v_pk_add_f32 v[244:245], v[120:121], v[244:245]
	v_exp_f32_e32 v125, v32
	v_exp_f32_e32 v126, v30
	v_pk_add_f32 v[244:245], v[122:123], v[244:245]
	v_exp_f32_e32 v103, v2
	v_exp_f32_e32 v106, v3
	v_pk_add_f32 v[244:245], v[124:125], v[244:245]
	v_exp_f32_e32 v107, v4
	v_add_f32_e32 v244, v126, v244
	v_exp_f32_e32 v110, v5
	v_exp_f32_e32 v111, v6
	v_exp_f32_e32 v114, v7
	v_pk_add_f32 v[244:245], v[106:107], v[244:245]
	v_exp_f32_e32 v115, v8
	v_exp_f32_e32 v117, v9
	v_pk_add_f32 v[244:245], v[110:111], v[244:245]
	v_exp_f32_e32 v102, v10
	v_exp_f32_e32 v104, v11
	v_pk_add_f32 v[244:245], v[114:115], v[244:245]
	v_exp_f32_e32 v105, v12
	v_exp_f32_e32 v108, v13
	v_pk_add_f32 v[244:245], v[102:103], v[244:245]
	v_exp_f32_e32 v109, v14
	v_exp_f32_e32 v112, v15
	v_pk_add_f32 v[244:245], v[104:105], v[244:245]
	v_exp_f32_e32 v113, v16
	v_exp_f32_e32 v116, v17
	v_pk_add_f32 v[244:245], v[108:109], v[244:245]
	v_exp_f32_e32 v72, v34
	v_exp_f32_e32 v75, v35
	v_pk_add_f32 v[244:245], v[112:113], v[244:245]
	v_exp_f32_e32 v76, v36
	v_pk_add_f32 v[244:245], v[116:117], v[244:245]
	v_exp_f32_e32 v79, v37
	v_exp_f32_e32 v80, v38
	v_exp_f32_e32 v98, v39
	v_exp_f32_e32 v99, v40
	v_exp_f32_e32 v101, v41
	v_exp_f32_e32 v71, v42
	v_exp_f32_e32 v73, v43
	v_pk_add_f32 v[244:245], v[98:99], v[244:245]
	v_exp_f32_e32 v74, v44
	v_exp_f32_e32 v77, v45
	v_exp_f32_e32 v78, v46
	v_pk_add_f32 v[244:245], v[72:73], v[244:245]
	v_exp_f32_e32 v81, v47
	v_pk_add_f32 v[244:245], v[74:75], v[244:245]
	v_exp_f32_e32 v97, v48
	v_pk_add_f32 v[244:245], v[76:77], v[244:245]
	v_exp_f32_e32 v100, v49
	v_pk_add_f32 v[244:245], v[78:79], v[244:245]
	v_exp_f32_e32 v41, v50
	v_pk_add_f32 v[244:245], v[80:81], v[244:245]
	v_exp_f32_e32 v46, v51
	v_add_f32_e32 v244, v97, v244
	v_exp_f32_e32 v47, v52
	v_pk_add_f32 v[244:245], v[100:101], v[244:245]
	v_exp_f32_e32 v53, v53
	v_exp_f32_e32 v54, v54
	v_exp_f32_e32 v67, v55
	v_pk_add_f32 v[244:245], v[46:47], v[244:245]
	v_exp_f32_e32 v68, v56
	v_exp_f32_e32 v69, v57
	v_exp_f32_e32 v38, v58
	v_add_f32_e32 v244, v67, v244
	v_exp_f32_e32 v44, v59
	v_exp_f32_e32 v45, v60
	v_pk_add_f32 v[244:245], v[68:69], v[244:245]
	v_exp_f32_e32 v51, v61
	v_exp_f32_e32 v52, v62
	v_exp_f32_e32 v57, v63
	v_pk_add_f32 v[244:245], v[44:45], v[244:245]
	v_exp_f32_e32 v58, v64
	v_exp_f32_e32 v62, v65
	v_pk_add_f32 v[244:245], v[52:53], v[244:245]
	v_exp_f32_e32 v37, v82
	v_exp_f32_e32 v42, v83
	v_add_f32_e32 v244, v58, v244
	v_exp_f32_e32 v43, v84
	v_exp_f32_e32 v49, v85
	v_exp_f32_e32 v50, v86
	v_exp_f32_e32 v55, v87
	v_pk_add_f32 v[244:245], v[42:43], v[244:245]
	v_exp_f32_e32 v56, v88
	v_exp_f32_e32 v61, v89
	v_pk_add_f32 v[244:245], v[50:51], v[244:245]
	v_exp_f32_e32 v36, v90
	v_pk_add_f32 v[244:245], v[54:55], v[244:245]
	v_exp_f32_e32 v39, v91
	v_pk_add_f32 v[244:245], v[56:57], v[244:245]
	v_exp_f32_e32 v40, v92
	v_add_f32_e32 v244, v61, v244
	v_pk_add_f32 v[244:245], v[36:37], v[244:245]
	v_pk_add_f32 v[244:245], v[38:39], v[244:245]
	v_pk_add_f32 v[244:245], v[40:41], v[244:245]
	v_exp_f32_e32 v48, v93
	v_cvt_pk_bf16_f32 v2, v33, v18
	v_cvt_pk_bf16_f32 v3, v19, v20
	v_cvt_pk_bf16_f32 v4, v21, v22
	v_cvt_pk_bf16_f32 v5, v23, v24
	ds_read_b64_tr_b16 v[228:229], v195
	ds_read_b64_tr_b16 v[230:231], v195 offset:1024
	ds_read_b64_tr_b16 v[232:233], v196
	ds_read_b64_tr_b16 v[234:235], v196 offset:1024
	s_waitcnt lgkmcnt(0)
	ds_read_b64_tr_b16 v[236:237], v197
	ds_read_b64_tr_b16 v[238:239], v197 offset:1024
	ds_read_b64_tr_b16 v[240:241], v198
	ds_read_b64_tr_b16 v[242:243], v198 offset:1024
	s_nop 0
	v_pk_add_f32 v[244:245], v[48:49], v[244:245]
	v_mfma_f32_32x32x16_bf16 v[18:33], v[228:231], v[2:5], 0
	v_exp_f32_e32 v63, v94
	v_exp_f32_e32 v65, v95
	v_exp_f32_e32 v64, v96
	v_mfma_f32_32x32x16_bf16 v[2:17], v[232:235], v[2:5], 0
	v_exp_f32_e32 v70, v70
	v_pk_add_f32 v[244:245], v[62:63], v[244:245]
	v_cvt_pk_bf16_f32 v82, v119, v120
	v_cvt_pk_bf16_f32 v83, v121, v122
	v_cvt_pk_bf16_f32 v84, v123, v124
	v_cvt_pk_bf16_f32 v85, v125, v126
	s_waitcnt lgkmcnt(0)
	ds_read_b64_tr_b16 v[228:229], v199
	ds_read_b64_tr_b16 v[230:231], v199 offset:1024
	ds_read_b64_tr_b16 v[232:233], v200
	ds_read_b64_tr_b16 v[234:235], v200 offset:1024
	v_mfma_f32_32x32x16_bf16 v[18:33], v[236:239], v[82:85], v[18:33]
	v_pk_add_f32 v[244:245], v[64:65], v[244:245]
	v_pk_add_f32 v[244:245], v[70:71], v[244:245]
	v_add_f32_e32 v59, v244, v245
	ds_bpermute_b32 v60, v118, v59
	v_mfma_f32_32x32x16_bf16 v[2:17], v[240:243], v[82:85], v[2:17]
